# router second sweep: the four rows' re-loads of one column chunk issued together (loads hoisted in the loop body, renamed, counted vmcnt)
# speedup vs baseline: 1.0247x; 1.0005x over previous
.LBB0_1031:
	v_lshl_add_u64 v[244:245], s[16:17], 0, v[40:41]
	global_load_dwordx4 v[130:133], v[244:245], off
	v_lshl_add_u64 v[134:135], v[84:85], 0, s[14:15]
	global_load_dwordx2 v[146:147], v[134:135], off
	v_lshl_add_u64 v[244:245], s[20:21], 0, v[40:41]
	global_load_dwordx4 v[138:141], v[244:245], off
	v_lshl_add_u64 v[142:143], s[18:19], 0, v[40:41]
	v_add_co_u32_e32 v136, vcc, 0x8000, v142
	s_nop 1
	v_addc_co_u32_e32 v137, vcc, 0, v143, vcc
	global_load_dwordx4 v[148:151], v[136:137], off
	v_add_co_u32_e32 v242, vcc, 0x6000, v142
	s_nop 1
	v_addc_co_u32_e32 v243, vcc, 0, v143, vcc
	global_load_dwordx4 v[152:155], v[242:243], off
	v_add_co_u32_e32 v136, vcc, s47, v244
	s_nop 1
	v_addc_co_u32_e32 v137, vcc, 0, v245, vcc
	v_add_co_u32_e32 v142, vcc, s47, v134
	s_nop 1
	v_addc_co_u32_e32 v143, vcc, 0, v135, vcc
	global_load_dwordx2 v[242:243], v[142:143], off offset:-4096
	global_load_dwordx4 v[158:161], v[136:137], off
	global_load_dwordx2 v[240:241], v[142:143], off
	v_add_co_u32_e32 v162, vcc, s49, v244
	s_nop 1
	v_addc_co_u32_e32 v163, vcc, 0, v245, vcc
	global_load_dwordx4 v[166:169], v[162:163], off
	v_add_co_u32_e32 v170, vcc, s9, v244
	s_nop 1
	v_addc_co_u32_e32 v171, vcc, 0, v245, vcc
	v_add_co_u32_e32 v164, vcc, s55, v134
	s_nop 1
	v_addc_co_u32_e32 v165, vcc, 0, v135, vcc
	global_load_dwordx2 v[162:163], v[164:165], off
	global_load_dwordx4 v[174:177], v[170:171], off
	v_lshl_add_u64 v[178:179], v[92:93], 0, s[14:15]
	s_waitcnt vmcnt(9)
	v_lshlrev_b32_e32 v172, 16, v146
	v_and_b32_e32 v173, 0xffff0000, v146
	v_lshlrev_b32_e32 v170, 16, v147
	v_and_b32_e32 v171, 0xffff0000, v147
	s_waitcnt vmcnt(8)
	v_pk_add_f32 v[164:165], v[138:139], v[172:173]
	v_pk_add_f32 v[156:157], v[140:141], v[170:171]
	s_waitcnt vmcnt(7)
	v_pk_add_f32 v[134:135], v[148:149], 1.0 op_sel_hi:[1,0]
	v_pk_add_f32 v[172:173], v[150:151], 1.0 op_sel_hi:[1,0]
	v_pk_mul_f32 v[170:171], v[0:1], v[164:165]
	v_pk_mul_f32 v[244:245], v[0:1], v[156:157]
	v_pk_mul_f32 v[146:147], v[130:131], v[134:135]
	v_pk_mul_f32 v[164:165], v[132:133], v[172:173]
	s_waitcnt vmcnt(6)
	v_pk_fma_f32 v[156:157], v[146:147], v[170:171], v[152:153]
	v_pk_fma_f32 v[238:239], v[164:165], v[244:245], v[154:155]
	v_cvt_pk_bf16_f32 v236, v156, v157
	v_cvt_pk_bf16_f32 v237, v238, v239
	global_store_dwordx2 v[178:179], v[236:237], off
	v_lshl_add_u64 v[172:173], v[90:91], 0, s[14:15]
	s_waitcnt vmcnt(6)
	v_lshlrev_b32_e32 v170, 16, v242
	v_and_b32_e32 v171, 0xffff0000, v242
	v_lshlrev_b32_e32 v178, 16, v243
	v_and_b32_e32 v179, 0xffff0000, v243
	s_waitcnt vmcnt(5)
	v_pk_add_f32 v[156:157], v[158:159], v[170:171]
	v_pk_add_f32 v[244:245], v[160:161], v[178:179]
	v_pk_mul_f32 v[242:243], v[2:3], v[156:157]
	v_pk_mul_f32 v[170:171], v[2:3], v[244:245]
	v_pk_fma_f32 v[178:179], v[146:147], v[242:243], v[152:153]
	v_pk_fma_f32 v[160:161], v[164:165], v[170:171], v[154:155]
	v_cvt_pk_bf16_f32 v244, v178, v179
	v_cvt_pk_bf16_f32 v245, v160, v161
	global_store_dwordx2 v[172:173], v[244:245], off
	v_lshl_add_u64 v[242:243], v[88:89], 0, s[14:15]
	s_waitcnt vmcnt(5)
	v_lshlrev_b32_e32 v178, 16, v240
	v_and_b32_e32 v179, 0xffff0000, v240
	v_lshlrev_b32_e32 v172, 16, v241
	v_and_b32_e32 v173, 0xffff0000, v241
	s_waitcnt vmcnt(4)
	v_pk_add_f32 v[170:171], v[166:167], v[178:179]
	v_pk_add_f32 v[160:161], v[168:169], v[172:173]
	v_pk_mul_f32 v[240:241], v[80:81], v[170:171]
	v_pk_mul_f32 v[178:179], v[80:81], v[160:161]
	v_pk_fma_f32 v[172:173], v[146:147], v[240:241], v[152:153]
	v_pk_fma_f32 v[166:167], v[164:165], v[178:179], v[154:155]
	v_cvt_pk_bf16_f32 v160, v172, v173
	v_cvt_pk_bf16_f32 v161, v166, v167
	global_store_dwordx2 v[242:243], v[160:161], off
	v_lshl_add_u64 v[178:179], v[86:87], 0, s[14:15]
	s_add_u32 s14, s14, 0x200
	s_addc_u32 s15, s15, 0
	s_add_u32 s20, s20, 0x400
	s_addc_u32 s21, s21, 0
	s_add_u32 s18, s18, 0x400
	s_addc_u32 s19, s19, 0
	s_add_u32 s16, s16, 0x400
	s_addc_u32 s17, s17, 0
	s_cmpk_eq_i32 s14, 0x1000
	s_waitcnt vmcnt(4)
	v_lshlrev_b32_e32 v172, 16, v162
	v_and_b32_e32 v173, 0xffff0000, v162
	v_lshlrev_b32_e32 v166, 16, v163
	v_and_b32_e32 v167, 0xffff0000, v163
	s_waitcnt vmcnt(3)
	v_pk_add_f32 v[244:245], v[174:175], v[172:173]
	v_pk_add_f32 v[130:131], v[176:177], v[166:167]
	v_pk_mul_f32 v[242:243], v[82:83], v[244:245]
	v_pk_mul_f32 v[240:241], v[82:83], v[130:131]
	v_pk_fma_f32 v[176:177], v[146:147], v[242:243], v[152:153]
	v_pk_fma_f32 v[166:167], v[164:165], v[240:241], v[154:155]
	v_cvt_pk_bf16_f32 v244, v176, v177
	v_cvt_pk_bf16_f32 v245, v166, v167
	global_store_dwordx2 v[178:179], v[244:245], off
	s_cbranch_scc0 .LBB0_1031
	v_mov_b32_e32 v1, v144
	s_nop 0
	v_and_b32_e32 v3, 32, v1
	v_lshlrev_b32_e32 v81, 2, v1
	v_cmp_eq_u32_e32 vcc, 0, v3
	v_xor_b32_e32 v83, 0x80, v81
	s_nop 0
	v_cndmask_b32_e32 v3, v78, v72, vcc
	ds_bpermute_b32 v3, v83, v3
	v_cndmask_b32_e32 v72, v72, v78, vcc
	v_cndmask_b32_e32 v78, v79, v73, vcc
	v_cndmask_b32_e32 v84, v76, v68, vcc
	v_cndmask_b32_e32 v68, v68, v76, vcc
	s_waitcnt lgkmcnt(0)
	v_add_f32_e32 v3, v72, v3
	v_cndmask_b32_e32 v72, v73, v79, vcc
	v_cndmask_b32_e32 v73, v77, v69, vcc
	ds_bpermute_b32 v73, v83, v73
	v_cndmask_b32_e32 v69, v69, v77, vcc
	v_cndmask_b32_e32 v76, v74, v60, vcc
	v_cndmask_b32_e32 v60, v60, v74, vcc
	v_cndmask_b32_e32 v74, v66, v54, vcc
	s_waitcnt lgkmcnt(0)
	v_add_f32_e32 v69, v69, v73
	v_cndmask_b32_e32 v73, v70, v56, vcc
	v_cndmask_b32_e32 v56, v56, v70, vcc
	ds_bpermute_b32 v70, v83, v73
	v_cndmask_b32_e32 v54, v54, v66, vcc
	v_cndmask_b32_e32 v66, v67, v55, vcc
	v_cndmask_b32_e32 v55, v55, v67, vcc
	v_cndmask_b32_e32 v67, v64, v50, vcc
	v_cndmask_b32_e32 v50, v50, v64, vcc
	v_cndmask_b32_e32 v64, v62, v46, vcc
	v_cndmask_b32_e32 v46, v46, v62, vcc
	ds_bpermute_b32 v62, v83, v64
	s_waitcnt lgkmcnt(1)
	v_add_f32_e32 v56, v56, v70
	v_cndmask_b32_e32 v70, v65, v51, vcc
	v_cndmask_b32_e32 v51, v51, v65, vcc
	v_cndmask_b32_e32 v65, v58, v30, vcc
	v_cndmask_b32_e32 v30, v30, v58, vcc
	v_cndmask_b32_e32 v58, v59, v31, vcc
	v_cndmask_b32_e32 v31, v31, v59, vcc
	v_cndmask_b32_e32 v59, v52, v28, vcc
	v_cndmask_b32_e32 v28, v28, v52, vcc
	v_cndmask_b32_e32 v52, v48, v24, vcc
	v_cndmask_b32_e32 v24, v24, v48, vcc
	ds_bpermute_b32 v48, v83, v52
	s_waitcnt lgkmcnt(1)
	v_add_f32_e32 v46, v46, v62
	v_cndmask_b32_e32 v62, v53, v29, vcc
	v_cndmask_b32_e32 v29, v29, v53, vcc
	v_cndmask_b32_e32 v53, v44, v22, vcc
	v_cndmask_b32_e32 v22, v22, v44, vcc
	v_cndmask_b32_e32 v44, v45, v23, vcc
	v_cndmask_b32_e32 v23, v23, v45, vcc
	v_cndmask_b32_e32 v45, v26, v18, vcc
	v_cndmask_b32_e32 v18, v18, v26, vcc
	v_cndmask_b32_e32 v26, v20, v14, vcc
	v_cndmask_b32_e32 v14, v14, v20, vcc
	ds_bpermute_b32 v20, v83, v26
	ds_bpermute_b32 v59, v83, v59
	s_waitcnt lgkmcnt(2)
	v_add_f32_e32 v24, v24, v48
	v_cndmask_b32_e32 v48, v27, v19, vcc
	v_cndmask_b32_e32 v19, v19, v27, vcc
	v_cndmask_b32_e32 v27, v16, v12, vcc
	v_cndmask_b32_e32 v12, v12, v16, vcc
	v_cndmask_b32_e32 v16, v17, v13, vcc
	ds_bpermute_b32 v16, v83, v16
	ds_bpermute_b32 v78, v83, v78
	ds_bpermute_b32 v62, v83, v62
	s_waitcnt lgkmcnt(4)
	v_add_f32_e32 v14, v14, v20
	v_cndmask_b32_e32 v13, v13, v17, vcc
	v_cndmask_b32_e32 v17, v10, v8, vcc
	v_cndmask_b32_e32 v20, v11, v9, vcc
	v_cndmask_b32_e32 v8, v8, v10, vcc
	v_cndmask_b32_e32 v9, v9, v11, vcc
	v_cndmask_b32_e32 v10, v6, v4, vcc
	v_and_b32_e32 v11, 16, v1
	ds_bpermute_b32 v84, v83, v84
	s_waitcnt lgkmcnt(4)
	v_add_f32_e32 v28, v28, v59
	v_cndmask_b32_e32 v52, v49, v25, vcc
	v_cndmask_b32_e32 v4, v4, v6, vcc
	ds_bpermute_b32 v6, v83, v10
	v_cndmask_b32_e32 v10, v7, v5, vcc
	v_cmp_eq_u32_e64 s[14:15], 0, v11
	ds_bpermute_b32 v52, v83, v52
	s_waitcnt lgkmcnt(5)
	v_add_f32_e32 v13, v13, v16
	ds_bpermute_b32 v10, v83, v10
	v_xor_b32_e32 v16, 64, v81
	v_cndmask_b32_e64 v11, v3, v28, s[14:15]
	ds_bpermute_b32 v11, v16, v11
	s_waitcnt lgkmcnt(6)
	v_add_f32_e32 v72, v72, v78
	s_waitcnt lgkmcnt(5)
	v_add_f32_e32 v29, v29, v62
	s_waitcnt lgkmcnt(4)
	v_add_f32_e32 v68, v68, v84
	v_cndmask_b32_e32 v25, v25, v49, vcc
	ds_bpermute_b32 v45, v83, v45
	s_waitcnt lgkmcnt(4)
	v_add_f32_e32 v4, v4, v6
	v_cndmask_b32_e32 v5, v5, v7, vcc
	v_cndmask_b32_e64 v6, v72, v29, s[14:15]
	s_waitcnt lgkmcnt(3)
	v_add_f32_e32 v25, v25, v52
	s_waitcnt lgkmcnt(2)
	v_add_f32_e32 v5, v5, v10
	v_cndmask_b32_e64 v3, v28, v3, s[14:15]
	ds_bpermute_b32 v6, v16, v6
	v_cndmask_b32_e64 v10, v68, v24, s[14:15]
	ds_bpermute_b32 v76, v83, v76
	v_cndmask_b32_e32 v77, v75, v61, vcc
	ds_bpermute_b32 v53, v83, v53
	s_waitcnt lgkmcnt(4)
	v_add_f32_e32 v3, v3, v11
	ds_bpermute_b32 v10, v16, v10
	v_cndmask_b32_e64 v11, v69, v25, s[14:15]
	ds_bpermute_b32 v77, v83, v77
	ds_bpermute_b32 v44, v83, v44
	ds_bpermute_b32 v11, v16, v11
	ds_bpermute_b32 v20, v83, v20
	s_waitcnt lgkmcnt(8)
	v_add_f32_e32 v18, v18, v45
	v_cndmask_b32_e64 v7, v29, v72, s[14:15]
	ds_bpermute_b32 v74, v83, v74
	v_cndmask_b32_e32 v26, v21, v15, vcc
	v_cndmask_b32_e32 v15, v15, v21, vcc
	s_waitcnt lgkmcnt(8)
	v_add_f32_e32 v6, v7, v6
	v_cndmask_b32_e64 v7, v24, v68, s[14:15]
	v_cndmask_b32_e64 v21, v56, v18, s[14:15]
	s_waitcnt lgkmcnt(7)
	v_add_f32_e32 v60, v60, v76
	v_cndmask_b32_e32 v61, v61, v75, vcc
	s_waitcnt lgkmcnt(6)
	v_add_f32_e32 v22, v22, v53
	s_waitcnt lgkmcnt(5)
	v_add_f32_e32 v7, v7, v10
	v_cndmask_b32_e64 v10, v25, v69, s[14:15]
	ds_bpermute_b32 v21, v16, v21
	s_waitcnt lgkmcnt(5)
	v_add_f32_e32 v61, v61, v77
	v_cndmask_b32_e32 v73, v71, v57, vcc
	s_waitcnt lgkmcnt(4)
	v_add_f32_e32 v23, v23, v44
	ds_bpermute_b32 v17, v83, v17
	s_waitcnt lgkmcnt(4)
	v_add_f32_e32 v10, v10, v11
	v_cndmask_b32_e64 v11, v60, v22, s[14:15]
	ds_bpermute_b32 v73, v83, v73
	ds_bpermute_b32 v66, v83, v66
	ds_bpermute_b32 v48, v83, v48
	ds_bpermute_b32 v26, v83, v26
	s_waitcnt lgkmcnt(7)
	v_add_f32_e32 v9, v9, v20
	ds_bpermute_b32 v11, v16, v11
	v_cndmask_b32_e64 v20, v61, v23, s[14:15]
	ds_bpermute_b32 v20, v16, v20
	s_waitcnt lgkmcnt(8)
	v_add_f32_e32 v54, v54, v74
	v_cndmask_b32_e64 v18, v18, v56, s[14:15]
	ds_bpermute_b32 v70, v83, v70
	s_waitcnt lgkmcnt(8)
	v_add_f32_e32 v18, v18, v21
	v_cndmask_b32_e64 v21, v54, v14, s[14:15]
	v_cndmask_b32_e32 v57, v57, v71, vcc
	s_waitcnt lgkmcnt(7)
	v_add_f32_e32 v8, v8, v17
	v_cndmask_b32_e64 v17, v22, v60, s[14:15]
	ds_bpermute_b32 v21, v16, v21
	s_waitcnt lgkmcnt(7)
	v_add_f32_e32 v57, v57, v73
	s_waitcnt lgkmcnt(6)
	v_add_f32_e32 v55, v55, v66
	s_waitcnt lgkmcnt(5)
	v_add_f32_e32 v19, v19, v48
	s_waitcnt lgkmcnt(4)
	v_add_f32_e32 v15, v15, v26
	s_waitcnt lgkmcnt(3)
	v_add_f32_e32 v11, v17, v11
	v_cndmask_b32_e64 v17, v23, v61, s[14:15]
	ds_bpermute_b32 v67, v83, v67
	ds_bpermute_b32 v27, v83, v27
	s_waitcnt lgkmcnt(4)
	v_add_f32_e32 v17, v17, v20
	v_cndmask_b32_e64 v20, v57, v19, s[14:15]
	v_cndmask_b32_e64 v22, v55, v15, s[14:15]
	ds_bpermute_b32 v20, v16, v20
	ds_bpermute_b32 v22, v16, v22
	s_waitcnt lgkmcnt(5)
	v_add_f32_e32 v51, v51, v70
	v_cndmask_b32_e64 v14, v14, v54, s[14:15]
	ds_bpermute_b32 v65, v83, v65
	s_waitcnt lgkmcnt(5)
	v_add_f32_e32 v14, v14, v21
	v_cndmask_b32_e64 v21, v51, v13, s[14:15]
	ds_bpermute_b32 v21, v16, v21
	s_waitcnt lgkmcnt(5)
	v_add_f32_e32 v50, v50, v67
	v_cndmask_b32_e32 v64, v63, v47, vcc
	s_waitcnt lgkmcnt(4)
	v_add_f32_e32 v12, v12, v27
	v_cndmask_b32_e64 v19, v19, v57, s[14:15]
	v_cndmask_b32_e64 v15, v15, v55, s[14:15]
	ds_bpermute_b32 v64, v83, v64
	ds_bpermute_b32 v58, v83, v58
	s_waitcnt lgkmcnt(5)
	v_add_f32_e32 v19, v19, v20
	s_waitcnt lgkmcnt(4)
	v_add_f32_e32 v15, v15, v22
	v_cndmask_b32_e64 v20, v50, v12, s[14:15]
	v_cndmask_b32_e64 v22, v46, v8, s[14:15]
	ds_bpermute_b32 v20, v16, v20
	ds_bpermute_b32 v22, v16, v22
	s_waitcnt lgkmcnt(5)
	v_add_f32_e32 v30, v30, v65
	v_cndmask_b32_e64 v13, v13, v51, s[14:15]
	s_waitcnt lgkmcnt(4)
	v_add_f32_e32 v13, v13, v21
	v_cndmask_b32_e64 v21, v30, v4, s[14:15]
	v_cndmask_b32_e32 v47, v47, v63, vcc
	ds_bpermute_b32 v21, v16, v21
	s_waitcnt lgkmcnt(4)
	v_add_f32_e32 v47, v47, v64
	s_waitcnt lgkmcnt(3)
	v_add_f32_e32 v31, v31, v58
	v_cndmask_b32_e64 v12, v12, v50, s[14:15]
	v_cndmask_b32_e64 v8, v8, v46, s[14:15]
	s_waitcnt lgkmcnt(2)
	v_add_f32_e32 v12, v12, v20
	s_waitcnt lgkmcnt(1)
	v_add_f32_e32 v8, v8, v22
	v_cndmask_b32_e64 v20, v47, v9, s[14:15]
	v_cndmask_b32_e64 v9, v9, v47, s[14:15]
	v_cndmask_b32_e64 v22, v31, v5, s[14:15]
	v_cndmask_b32_e64 v4, v4, v30, s[14:15]
	v_cndmask_b32_e64 v5, v5, v31, s[14:15]
	s_load_dwordx2 s[14:15], s[22:23], 0x1b8
	s_waitcnt lgkmcnt(0)
	v_add_f32_e32 v4, v4, v21
	v_and_b32_e32 v21, 15, v1
	v_lshlrev_b32_e32 v21, 2, v21
	ds_bpermute_b32 v20, v16, v20
	global_load_dword v21, v21, s[14:15]
	ds_bpermute_b32 v16, v16, v22
	s_waitcnt lgkmcnt(1)
	v_add_f32_e32 v9, v9, v20
	v_xor_b32_e32 v20, 32, v81
	s_waitcnt lgkmcnt(0)
	v_add_f32_e32 v5, v5, v16
	v_and_b32_e32 v16, 8, v1
	v_cmp_eq_u32_e32 vcc, 0, v16
	s_nop 1
	v_cndmask_b32_e32 v16, v3, v14, vcc
	v_cndmask_b32_e32 v22, v7, v12, vcc
	v_cndmask_b32_e32 v7, v12, v7, vcc
	v_cndmask_b32_e32 v12, v10, v13, vcc
	v_cndmask_b32_e32 v3, v14, v3, vcc
	ds_bpermute_b32 v14, v20, v16
	ds_bpermute_b32 v12, v20, v12
	v_cndmask_b32_e32 v10, v13, v10, vcc
	v_cndmask_b32_e32 v13, v11, v8, vcc
	v_cndmask_b32_e32 v16, v6, v15, vcc
	s_waitcnt lgkmcnt(1)
	v_add_f32_e32 v3, v3, v14
	ds_bpermute_b32 v13, v20, v13
	v_cndmask_b32_e32 v14, v17, v9, vcc
	s_waitcnt lgkmcnt(1)
	v_add_f32_e32 v10, v10, v12
	v_cndmask_b32_e32 v8, v8, v11, vcc
	v_cndmask_b32_e32 v11, v18, v4, vcc
	v_cndmask_b32_e32 v12, v19, v5, vcc
	ds_bpermute_b32 v16, v20, v16
	ds_bpermute_b32 v22, v20, v22
	ds_bpermute_b32 v14, v20, v14
	ds_bpermute_b32 v11, v20, v11
	ds_bpermute_b32 v12, v20, v12
	v_cndmask_b32_e32 v6, v15, v6, vcc
	s_waitcnt lgkmcnt(5)
	v_add_f32_e32 v8, v8, v13
	v_cndmask_b32_e32 v9, v9, v17, vcc
	v_cndmask_b32_e32 v4, v4, v18, vcc
	v_and_b32_e32 v13, 4, v1
	v_cndmask_b32_e32 v5, v5, v19, vcc
	s_waitcnt lgkmcnt(4)
	v_add_f32_e32 v6, v6, v16
	s_waitcnt lgkmcnt(3)
	v_add_f32_e32 v7, v7, v22
	s_waitcnt lgkmcnt(2)
	v_add_f32_e32 v9, v9, v14
	v_cmp_eq_u32_e64 s[14:15], 0, v13
	s_waitcnt lgkmcnt(1)
	v_add_f32_e32 v4, v4, v11
	s_waitcnt lgkmcnt(0)
	v_add_f32_e32 v5, v5, v12
	v_xor_b32_e32 v14, 16, v81
	v_cndmask_b32_e64 v13, v3, v8, s[14:15]
	v_cndmask_b32_e64 v3, v8, v3, s[14:15]
	v_cndmask_b32_e64 v8, v6, v9, s[14:15]
	v_cndmask_b32_e64 v6, v9, v6, s[14:15]
	v_cndmask_b32_e64 v9, v7, v4, s[14:15]
	v_cndmask_b32_e64 v11, v10, v5, s[14:15]
	ds_bpermute_b32 v13, v14, v13
	ds_bpermute_b32 v8, v14, v8
	ds_bpermute_b32 v9, v14, v9
	ds_bpermute_b32 v11, v14, v11
	v_cndmask_b32_e64 v4, v4, v7, s[14:15]
	v_cndmask_b32_e64 v5, v5, v10, s[14:15]
	v_and_b32_e32 v7, 2, v1
	s_waitcnt lgkmcnt(3)
	v_add_f32_e32 v3, v3, v13
	s_waitcnt lgkmcnt(2)
	v_add_f32_e32 v6, v6, v8
	s_waitcnt lgkmcnt(1)
	v_add_f32_e32 v4, v4, v9
	s_waitcnt lgkmcnt(0)
	v_add_f32_e32 v5, v5, v11
	v_cmp_eq_u32_e32 vcc, 0, v7
	v_xor_b32_e32 v8, 8, v81
	s_nop 0
	v_cndmask_b32_e32 v7, v3, v4, vcc
	v_cndmask_b32_e32 v9, v6, v5, vcc
	ds_bpermute_b32 v7, v8, v7
	ds_bpermute_b32 v8, v8, v9
	v_cndmask_b32_e32 v3, v4, v3, vcc
	v_cndmask_b32_e32 v4, v5, v6, vcc
	v_and_b32_e32 v6, 1, v1
	s_waitcnt lgkmcnt(1)
	v_add_f32_e32 v3, v3, v7
	s_waitcnt lgkmcnt(0)
	v_add_f32_e32 v4, v4, v8
	v_cmp_eq_u32_e32 vcc, 0, v6
	v_xor_b32_e32 v5, 4, v81
	s_nop 0
	v_cndmask_b32_e32 v6, v3, v4, vcc
	ds_bpermute_b32 v5, v5, v6
	v_cndmask_b32_e32 v3, v4, v3, vcc
	v_ashrrev_i32_e32 v4, 4, v1
	v_cmp_eq_u32_e32 vcc, 2, v4
	s_waitcnt lgkmcnt(0)
	v_add_f32_e32 v3, v3, v5
	v_cndmask_b32_e32 v5, v82, v80, vcc
	v_cmp_eq_u32_e32 vcc, 1, v4
	s_nop 1
	v_cndmask_b32_e32 v2, v5, v2, vcc
	v_cmp_gt_u32_e32 vcc, 16, v1
	s_nop 1
	v_cndmask_b32_e32 v0, v2, v0, vcc
	s_waitcnt vmcnt(0)
	v_fmac_f32_e32 v21, v0, v3
	v_add_u32_e32 v0, s96, v81
	ds_write_b32 v0, v21
	s_waitcnt lgkmcnt(0)
	s_and_saveexec_b64 s[50:51], s[12:13]
	s_cbranch_execz .LBB0_1172
	s_load_dwordx2 s[14:15], s[22:23], 0xa8
	v_add_u32_e32 v4, s96, v103
	s_waitcnt lgkmcnt(0)
	global_load_dwordx4 v[24:27], v33, s[14:15]
	global_load_dwordx4 v[16:19], v33, s[14:15] offset:16
	global_load_dwordx4 v[0:3], v33, s[14:15] offset:48
	global_load_dwordx4 v[8:11], v33, s[14:15] offset:32
	ds_read_b128 v[28:31], v4
	ds_read_b128 v[20:23], v4 offset:16
	s_waitcnt lgkmcnt(1)
	v_mul_f32_e32 v5, 0xbfb8aa3b, v28
	v_exp_f32_e32 v28, v5
	v_mul_f32_e32 v6, 0xbfb8aa3b, v29
	v_exp_f32_e32 v29, v6
	ds_read_b128 v[12:15], v4 offset:32
	ds_read_b128 v[4:7], v4 offset:48
	v_add_f32_e32 v28, 1.0, v28
	v_div_scale_f32 v44, s[14:15], v28, v28, 1.0
	v_add_f32_e32 v29, 1.0, v29
	v_rcp_f32_e32 v47, v44
	v_div_scale_f32 v46, s[14:15], v29, v29, 1.0
	v_rcp_f32_e32 v49, v46
	v_fma_f32 v50, -v44, v47, 1.0
	v_div_scale_f32 v45, vcc, 1.0, v28, 1.0
	v_fmac_f32_e32 v47, v50, v47
	v_fma_f32 v51, -v46, v49, 1.0
	v_mul_f32_e32 v50, v45, v47
	v_div_scale_f32 v48, s[14:15], 1.0, v29, 1.0
	v_fmac_f32_e32 v49, v51, v49
	v_fma_f32 v52, -v44, v50, v45
	v_mul_f32_e32 v51, v48, v49
	v_fmac_f32_e32 v50, v52, v47
	v_fma_f32 v53, -v46, v51, v48
	v_fma_f32 v44, -v44, v50, v45
	v_fmac_f32_e32 v51, v53, v49
	v_div_fmas_f32 v44, v44, v47, v50
	v_fma_f32 v45, -v46, v51, v48
	v_div_fixup_f32 v48, v44, v28, 1.0
	s_mov_b64 vcc, s[14:15]
	v_div_fmas_f32 v28, v45, v49, v51
	v_div_fixup_f32 v46, v28, v29, 1.0
	s_waitcnt vmcnt(3)
	v_add_f32_e32 v49, v24, v48
	v_cmp_lt_f32_e64 s[14:15], s57, v49
	v_add_f32_e32 v47, v25, v46
	v_mov_b32_e32 v24, v47
	v_cndmask_b32_e64 v25, v110, v49, s[14:15]
	v_cmp_ngt_f32_e32 vcc, v47, v25
	s_and_saveexec_b64 s[16:17], vcc
	s_cbranch_execz .LBB0_1037
	v_mov_b32_e32 v28, 0xf149f2ca
	v_cmp_gt_f32_e32 vcc, v47, v28
	s_and_saveexec_b64 s[18:19], vcc
	v_mov_b32_e32 v28, v47
	s_or_b64 exec, exec, s[18:19]
	v_mov_b32_e32 v24, v25
	v_mov_b32_e32 v25, v28

.LBB0_2422:
	global_load_dwordx4 v[130:133], v[96:97], off
	v_lshl_add_u64 v[134:135], v[86:87], 0, s[10:11]
	global_load_dwordx2 v[244:245], v[134:135], off
	v_lshl_add_u64 v[146:147], v[84:85], 0, s[10:11]
	global_load_dwordx2 v[242:243], v[146:147], off
	v_add_co_u32_e32 v240, vcc, 0x2000, v98
	s_nop 1
	v_addc_co_u32_e32 v241, vcc, 0, v99, vcc
	global_load_dwordx4 v[138:141], v[240:241], off
	global_load_dwordx4 v[150:153], v[98:99], off
	v_add_co_u32_e32 v154, vcc, s39, v134
	s_nop 1
	v_addc_co_u32_e32 v155, vcc, 0, v135, vcc
	global_load_dwordx2 v[240:241], v[154:155], off offset:-4096
	v_add_co_u32_e32 v148, vcc, s39, v146
	s_nop 1
	v_addc_co_u32_e32 v149, vcc, 0, v147, vcc
	global_load_dwordx2 v[142:143], v[148:149], off offset:-4096
	global_load_dwordx2 v[136:137], v[154:155], off
	global_load_dwordx2 v[238:239], v[148:149], off
	v_add_co_u32_e32 v236, vcc, s41, v134
	s_nop 1
	v_addc_co_u32_e32 v237, vcc, 0, v135, vcc
	global_load_dwordx2 v[154:155], v[236:237], off
	v_add_co_u32_e32 v148, vcc, s41, v146
	s_nop 1
	v_addc_co_u32_e32 v149, vcc, 0, v147, vcc
	global_load_dwordx2 v[236:237], v[148:149], off
	v_lshl_add_u64 v[134:135], v[94:95], 0, s[10:11]
	v_lshl_add_u64 v[96:97], v[96:97], 0, s[42:43]
	v_lshl_add_u64 v[98:99], v[98:99], 0, s[42:43]
	s_waitcnt vmcnt(9)
	v_lshlrev_b32_e32 v148, 16, v244
	v_and_b32_e32 v149, 0xffff0000, v244
	s_waitcnt vmcnt(8)
	v_lshlrev_b32_e32 v146, 16, v242
	v_and_b32_e32 v147, 0xffff0000, v242
	v_lshlrev_b32_e32 v234, 16, v245
	v_and_b32_e32 v235, 0xffff0000, v245
	v_lshlrev_b32_e32 v232, 16, v243
	v_and_b32_e32 v233, 0xffff0000, v243
	v_pk_add_f32 v[244:245], v[148:149], v[146:147]
	s_waitcnt vmcnt(7)
	v_pk_add_f32 v[230:231], v[138:139], 1.0 op_sel_hi:[1,0]
	v_pk_add_f32 v[242:243], v[234:235], v[232:233]
	v_pk_add_f32 v[228:229], v[140:141], 1.0 op_sel_hi:[1,0]
	v_pk_mul_f32 v[148:149], v[76:77], v[244:245]
	v_pk_mul_f32 v[146:147], v[130:131], v[230:231]
	v_pk_mul_f32 v[140:141], v[76:77], v[242:243]
	v_pk_mul_f32 v[138:139], v[132:133], v[228:229]
	s_waitcnt vmcnt(6)
	v_pk_fma_f32 v[244:245], v[146:147], v[148:149], v[150:151]
	v_pk_fma_f32 v[242:243], v[138:139], v[140:141], v[152:153]
	v_cvt_pk_bf16_f32 v132, v244, v245
	v_cvt_pk_bf16_f32 v133, v242, v243
	global_store_dwordx2 v[134:135], v[132:133], off
	v_lshl_add_u64 v[148:149], v[92:93], 0, s[10:11]
	s_waitcnt vmcnt(6)
	v_lshlrev_b32_e32 v242, 16, v240
	v_and_b32_e32 v243, 0xffff0000, v240
	s_waitcnt vmcnt(5)
	v_lshlrev_b32_e32 v140, 16, v142
	v_and_b32_e32 v141, 0xffff0000, v142
	v_lshlrev_b32_e32 v244, 16, v241
	v_and_b32_e32 v245, 0xffff0000, v241
	v_lshlrev_b32_e32 v130, 16, v143
	v_and_b32_e32 v131, 0xffff0000, v143
	v_pk_add_f32 v[240:241], v[242:243], v[140:141]
	v_pk_add_f32 v[234:235], v[244:245], v[130:131]
	v_pk_mul_f32 v[232:233], v[78:79], v[240:241]
	v_pk_mul_f32 v[242:243], v[78:79], v[234:235]
	v_pk_fma_f32 v[244:245], v[146:147], v[232:233], v[150:151]
	v_pk_fma_f32 v[240:241], v[138:139], v[242:243], v[152:153]
	v_cvt_pk_bf16_f32 v130, v244, v245
	v_cvt_pk_bf16_f32 v131, v240, v241
	global_store_dwordx2 v[148:149], v[130:131], off
	v_lshl_add_u64 v[244:245], v[90:91], 0, s[10:11]
	s_waitcnt vmcnt(5)
	v_lshlrev_b32_e32 v242, 16, v136
	v_and_b32_e32 v243, 0xffff0000, v136
	s_waitcnt vmcnt(4)
	v_lshlrev_b32_e32 v240, 16, v238
	v_and_b32_e32 v241, 0xffff0000, v238
	v_lshlrev_b32_e32 v148, 16, v137
	v_and_b32_e32 v149, 0xffff0000, v137
	v_lshlrev_b32_e32 v130, 16, v239
	v_and_b32_e32 v131, 0xffff0000, v239
	v_pk_add_f32 v[136:137], v[242:243], v[240:241]
	v_pk_add_f32 v[234:235], v[148:149], v[130:131]
	v_pk_mul_f32 v[238:239], v[80:81], v[136:137]
	v_pk_mul_f32 v[232:233], v[80:81], v[234:235]
	v_pk_fma_f32 v[148:149], v[146:147], v[238:239], v[150:151]
	v_pk_fma_f32 v[136:137], v[138:139], v[232:233], v[152:153]
	v_cvt_pk_bf16_f32 v130, v148, v149
	v_cvt_pk_bf16_f32 v131, v136, v137
	global_store_dwordx2 v[244:245], v[130:131], off
	v_lshl_add_u64 v[238:239], v[88:89], 0, s[10:11]
	s_add_u32 s10, s10, 0x200
	s_addc_u32 s11, s11, 0
	s_cmpk_eq_i32 s10, 0x1000
	s_waitcnt vmcnt(4)
	v_lshlrev_b32_e32 v148, 16, v154
	v_and_b32_e32 v149, 0xffff0000, v154
	s_waitcnt vmcnt(3)
	v_lshlrev_b32_e32 v136, 16, v236
	v_and_b32_e32 v137, 0xffff0000, v236
	v_lshlrev_b32_e32 v244, 16, v155
	v_and_b32_e32 v245, 0xffff0000, v155
	v_lshlrev_b32_e32 v130, 16, v237
	v_and_b32_e32 v131, 0xffff0000, v237
	v_pk_add_f32 v[154:155], v[148:149], v[136:137]
	v_pk_add_f32 v[242:243], v[244:245], v[130:131]
	v_pk_mul_f32 v[240:241], v[82:83], v[154:155]
	v_pk_mul_f32 v[236:237], v[82:83], v[242:243]
	v_pk_fma_f32 v[148:149], v[146:147], v[240:241], v[150:151]
	v_pk_fma_f32 v[154:155], v[138:139], v[236:237], v[152:153]
	v_cvt_pk_bf16_f32 v244, v148, v149
	v_cvt_pk_bf16_f32 v245, v154, v155
	global_store_dwordx2 v[238:239], v[244:245], off
	s_cbranch_scc0 .LBB0_2422
	v_mov_b32_e32 v77, v144
	s_nop 0
	v_and_b32_e32 v79, 32, v77
	v_lshlrev_b32_e32 v81, 2, v77
	v_cmp_eq_u32_e32 vcc, 0, v79
	v_xor_b32_e32 v83, 0x80, v81
	s_nop 0
	v_cndmask_b32_e32 v79, v74, v68, vcc
	v_cndmask_b32_e32 v68, v68, v74, vcc
	ds_bpermute_b32 v74, v83, v79
	v_cndmask_b32_e32 v84, v72, v64, vcc
	v_cndmask_b32_e32 v64, v64, v72, vcc
	v_cndmask_b32_e32 v72, v73, v65, vcc
	v_cndmask_b32_e32 v65, v65, v73, vcc
	v_cndmask_b32_e32 v73, v70, v56, vcc
	v_cndmask_b32_e32 v56, v56, v70, vcc
	v_cndmask_b32_e32 v70, v66, v52, vcc
	v_cndmask_b32_e32 v52, v52, v66, vcc
	ds_bpermute_b32 v66, v83, v70
	s_waitcnt lgkmcnt(1)
	v_add_f32_e32 v68, v68, v74
	v_cndmask_b32_e32 v74, v71, v57, vcc
	v_cndmask_b32_e32 v57, v57, v71, vcc
	v_cndmask_b32_e32 v71, v62, v50, vcc
	v_cndmask_b32_e32 v50, v50, v62, vcc
	v_cndmask_b32_e32 v62, v63, v51, vcc
	v_cndmask_b32_e32 v51, v51, v63, vcc
	v_cndmask_b32_e32 v63, v60, v46, vcc
	v_cndmask_b32_e32 v46, v46, v60, vcc
	v_cndmask_b32_e32 v60, v58, v30, vcc
	v_cndmask_b32_e32 v30, v30, v58, vcc
	ds_bpermute_b32 v58, v83, v60
	s_waitcnt lgkmcnt(1)
	v_add_f32_e32 v52, v52, v66
	v_cndmask_b32_e32 v66, v61, v47, vcc
	v_cndmask_b32_e32 v47, v47, v61, vcc
	v_cndmask_b32_e32 v61, v54, v26, vcc
	v_cndmask_b32_e32 v26, v26, v54, vcc
	v_cndmask_b32_e32 v54, v55, v27, vcc
	v_cndmask_b32_e32 v27, v27, v55, vcc
	v_cndmask_b32_e32 v55, v48, v24, vcc
	v_cndmask_b32_e32 v24, v24, v48, vcc
	v_cndmask_b32_e32 v48, v44, v20, vcc
	v_cndmask_b32_e32 v20, v20, v44, vcc
	ds_bpermute_b32 v44, v83, v48
	s_waitcnt lgkmcnt(1)
	v_add_f32_e32 v30, v30, v58
	v_cndmask_b32_e32 v58, v49, v25, vcc
	v_cndmask_b32_e32 v25, v25, v49, vcc
	v_cndmask_b32_e32 v49, v28, v18, vcc
	v_cndmask_b32_e32 v18, v18, v28, vcc
	v_cndmask_b32_e32 v28, v29, v19, vcc
	v_cndmask_b32_e32 v19, v19, v29, vcc
	v_cndmask_b32_e32 v29, v22, v14, vcc
	v_cndmask_b32_e32 v14, v14, v22, vcc
	v_cndmask_b32_e32 v22, v16, v10, vcc
	v_cndmask_b32_e32 v10, v10, v16, vcc
	ds_bpermute_b32 v16, v83, v22
	ds_bpermute_b32 v55, v83, v55
	s_waitcnt lgkmcnt(2)
	v_add_f32_e32 v20, v20, v44
	v_cndmask_b32_e32 v44, v23, v15, vcc
	v_cndmask_b32_e32 v15, v15, v23, vcc
	v_cndmask_b32_e32 v23, v12, v8, vcc
	v_cndmask_b32_e32 v8, v8, v12, vcc
	v_cndmask_b32_e32 v12, v13, v9, vcc
	ds_bpermute_b32 v12, v83, v12
	v_cndmask_b32_e32 v79, v75, v69, vcc
	s_waitcnt lgkmcnt(2)
	v_add_f32_e32 v10, v10, v16
	v_cndmask_b32_e32 v16, v7, v5, vcc
	v_cndmask_b32_e32 v5, v5, v7, vcc
	v_and_b32_e32 v7, 16, v77
	ds_bpermute_b32 v79, v83, v79
	ds_bpermute_b32 v58, v83, v58
	s_waitcnt lgkmcnt(3)
	v_add_f32_e32 v24, v24, v55
	v_cndmask_b32_e32 v9, v9, v13, vcc
	v_cndmask_b32_e32 v13, v6, v4, vcc
	v_cndmask_b32_e32 v4, v4, v6, vcc
	v_cndmask_b32_e32 v6, v2, v0, vcc
	v_cmp_eq_u32_e64 s[10:11], 0, v7
	ds_bpermute_b32 v84, v83, v84
	v_cndmask_b32_e32 v48, v45, v21, vcc
	s_waitcnt lgkmcnt(3)
	v_add_f32_e32 v9, v9, v12
	v_cndmask_b32_e32 v0, v0, v2, vcc
	ds_bpermute_b32 v2, v83, v6
	v_xor_b32_e32 v12, 64, v81
	v_cndmask_b32_e64 v7, v68, v24, s[10:11]
	ds_bpermute_b32 v72, v83, v72
	ds_bpermute_b32 v48, v83, v48
	ds_bpermute_b32 v7, v12, v7
	ds_bpermute_b32 v13, v83, v13
	v_cndmask_b32_e32 v69, v69, v75, vcc
	s_waitcnt lgkmcnt(7)
	v_add_f32_e32 v69, v69, v79
	s_waitcnt lgkmcnt(6)
	v_add_f32_e32 v25, v25, v58
	v_cndmask_b32_e32 v6, v3, v1, vcc
	s_waitcnt lgkmcnt(5)
	v_add_f32_e32 v64, v64, v84
	v_cndmask_b32_e32 v21, v21, v45, vcc
	ds_bpermute_b32 v6, v83, v6
	s_waitcnt lgkmcnt(5)
	v_add_f32_e32 v0, v0, v2
	v_cndmask_b32_e32 v1, v1, v3, vcc
	v_cndmask_b32_e64 v2, v24, v68, s[10:11]
	v_cndmask_b32_e64 v3, v69, v25, s[10:11]
	s_waitcnt lgkmcnt(4)
	v_add_f32_e32 v65, v65, v72
	s_waitcnt lgkmcnt(3)
	v_add_f32_e32 v21, v21, v48
	s_waitcnt lgkmcnt(2)
	v_add_f32_e32 v2, v2, v7
	ds_bpermute_b32 v3, v12, v3
	v_cndmask_b32_e64 v7, v64, v20, s[10:11]
	ds_bpermute_b32 v73, v83, v73
	ds_bpermute_b32 v49, v83, v49
	ds_bpermute_b32 v29, v83, v29
	s_waitcnt lgkmcnt(5)
	v_add_f32_e32 v4, v4, v13
	ds_bpermute_b32 v7, v12, v7
	v_cndmask_b32_e64 v13, v65, v21, s[10:11]
	ds_bpermute_b32 v16, v83, v16
	ds_bpermute_b32 v13, v12, v13
	ds_bpermute_b32 v74, v83, v74
	ds_bpermute_b32 v28, v83, v28
	s_waitcnt lgkmcnt(9)
	v_add_f32_e32 v1, v1, v6
	v_cndmask_b32_e64 v6, v25, v69, s[10:11]
	s_waitcnt lgkmcnt(8)
	v_add_f32_e32 v3, v6, v3
	v_cndmask_b32_e64 v6, v20, v64, s[10:11]
	s_waitcnt lgkmcnt(7)
	v_add_f32_e32 v56, v56, v73
	s_waitcnt lgkmcnt(6)
	v_add_f32_e32 v18, v18, v49
	s_waitcnt lgkmcnt(5)
	v_add_f32_e32 v14, v14, v29
	s_waitcnt lgkmcnt(4)
	v_add_f32_e32 v6, v6, v7
	v_cndmask_b32_e64 v7, v21, v65, s[10:11]
	ds_bpermute_b32 v71, v83, v71
	s_waitcnt lgkmcnt(4)
	v_add_f32_e32 v5, v5, v16
	s_waitcnt lgkmcnt(3)
	v_add_f32_e32 v7, v7, v13
	v_cndmask_b32_e64 v13, v56, v18, s[10:11]
	v_cndmask_b32_e64 v16, v18, v56, s[10:11]
	v_cndmask_b32_e64 v18, v52, v14, s[10:11]
	ds_bpermute_b32 v18, v12, v18
	s_waitcnt lgkmcnt(3)
	v_add_f32_e32 v57, v57, v74
	v_cndmask_b32_e32 v70, v67, v53, vcc
	s_waitcnt lgkmcnt(2)
	v_add_f32_e32 v19, v19, v28
	v_cndmask_b32_e32 v22, v17, v11, vcc
	ds_bpermute_b32 v70, v83, v70
	ds_bpermute_b32 v62, v83, v62
	ds_bpermute_b32 v44, v83, v44
	ds_bpermute_b32 v22, v83, v22
	v_cndmask_b32_e32 v11, v11, v17, vcc
	ds_bpermute_b32 v13, v12, v13
	v_cndmask_b32_e64 v17, v57, v19, s[10:11]
	ds_bpermute_b32 v17, v12, v17
	s_waitcnt lgkmcnt(7)
	v_add_f32_e32 v50, v50, v71
	v_cndmask_b32_e64 v14, v14, v52, s[10:11]
	ds_bpermute_b32 v66, v83, v66
	s_waitcnt lgkmcnt(7)
	v_add_f32_e32 v14, v14, v18
	v_cndmask_b32_e64 v18, v50, v10, s[10:11]
	v_cndmask_b32_e32 v53, v53, v67, vcc
	ds_bpermute_b32 v18, v12, v18
	s_waitcnt lgkmcnt(7)
	v_add_f32_e32 v53, v53, v70
	s_waitcnt lgkmcnt(6)
	v_add_f32_e32 v51, v51, v62
	s_waitcnt lgkmcnt(5)
	v_add_f32_e32 v15, v15, v44
	s_waitcnt lgkmcnt(4)
	v_add_f32_e32 v11, v11, v22
	s_waitcnt lgkmcnt(3)
	v_add_f32_e32 v13, v16, v13
	v_cndmask_b32_e64 v16, v19, v57, s[10:11]
	ds_bpermute_b32 v63, v83, v63
	ds_bpermute_b32 v23, v83, v23
	s_waitcnt lgkmcnt(4)
	v_add_f32_e32 v16, v16, v17
	v_cndmask_b32_e64 v17, v53, v15, s[10:11]
	v_cndmask_b32_e64 v19, v51, v11, s[10:11]
	ds_bpermute_b32 v17, v12, v17
	ds_bpermute_b32 v19, v12, v19
	s_waitcnt lgkmcnt(5)
	v_add_f32_e32 v47, v47, v66
	v_cndmask_b32_e64 v10, v10, v50, s[10:11]
	ds_bpermute_b32 v61, v83, v61
	s_waitcnt lgkmcnt(5)
	v_add_f32_e32 v10, v10, v18
	v_cndmask_b32_e64 v18, v47, v9, s[10:11]
	ds_bpermute_b32 v18, v12, v18
	s_waitcnt lgkmcnt(5)
	v_add_f32_e32 v46, v46, v63
	v_cndmask_b32_e32 v60, v59, v31, vcc
	s_waitcnt lgkmcnt(4)
	v_add_f32_e32 v8, v8, v23
	v_cndmask_b32_e64 v15, v15, v53, s[10:11]
	v_cndmask_b32_e64 v11, v11, v51, s[10:11]
	ds_bpermute_b32 v60, v83, v60
	ds_bpermute_b32 v54, v83, v54
	s_waitcnt lgkmcnt(5)
	v_add_f32_e32 v15, v15, v17
	s_waitcnt lgkmcnt(4)
	v_add_f32_e32 v11, v11, v19
	v_cndmask_b32_e64 v17, v46, v8, s[10:11]
	v_cndmask_b32_e64 v19, v30, v4, s[10:11]
	ds_bpermute_b32 v17, v12, v17
	ds_bpermute_b32 v19, v12, v19
	s_waitcnt lgkmcnt(5)
	v_add_f32_e32 v26, v26, v61
	v_cndmask_b32_e64 v9, v9, v47, s[10:11]
	s_waitcnt lgkmcnt(4)
	v_add_f32_e32 v9, v9, v18
	v_cndmask_b32_e64 v18, v26, v0, s[10:11]
	v_cndmask_b32_e32 v31, v31, v59, vcc
	ds_bpermute_b32 v18, v12, v18
	s_waitcnt lgkmcnt(4)
	v_add_f32_e32 v31, v31, v60
	s_waitcnt lgkmcnt(3)
	v_add_f32_e32 v27, v27, v54
	v_cndmask_b32_e64 v8, v8, v46, s[10:11]
	v_cndmask_b32_e64 v4, v4, v30, s[10:11]
	s_waitcnt lgkmcnt(2)
	v_add_f32_e32 v8, v8, v17
	s_waitcnt lgkmcnt(1)
	v_add_f32_e32 v4, v4, v19
	v_cndmask_b32_e64 v17, v31, v5, s[10:11]
	v_cndmask_b32_e64 v5, v5, v31, s[10:11]
	v_cndmask_b32_e64 v19, v27, v1, s[10:11]
	v_cndmask_b32_e64 v0, v0, v26, s[10:11]
	v_cndmask_b32_e64 v1, v1, v27, s[10:11]
	s_load_dwordx2 s[10:11], s[18:19], 0x1b8
	s_waitcnt lgkmcnt(0)
	v_add_f32_e32 v0, v0, v18
	v_and_b32_e32 v18, 15, v77
	v_lshlrev_b32_e32 v18, 2, v18
	ds_bpermute_b32 v17, v12, v17
	global_load_dword v18, v18, s[10:11] offset:64
	ds_bpermute_b32 v12, v12, v19
	s_waitcnt lgkmcnt(1)
	v_add_f32_e32 v5, v5, v17
	v_xor_b32_e32 v17, 32, v81
	s_waitcnt lgkmcnt(0)
	v_add_f32_e32 v1, v1, v12
	v_and_b32_e32 v12, 8, v77
	v_cmp_eq_u32_e32 vcc, 0, v12
	s_nop 1
	v_cndmask_b32_e32 v12, v2, v10, vcc
	v_cndmask_b32_e32 v2, v10, v2, vcc
	ds_bpermute_b32 v10, v17, v12
	v_cndmask_b32_e32 v19, v6, v8, vcc
	v_cndmask_b32_e32 v6, v8, v6, vcc
	v_cndmask_b32_e32 v8, v7, v9, vcc
	v_cndmask_b32_e32 v7, v9, v7, vcc
	v_cndmask_b32_e32 v9, v13, v4, vcc
	ds_bpermute_b32 v8, v17, v8
	ds_bpermute_b32 v9, v17, v9
	s_waitcnt lgkmcnt(2)
	v_add_f32_e32 v2, v2, v10
	v_cndmask_b32_e32 v10, v16, v5, vcc
	v_cndmask_b32_e32 v12, v3, v11, vcc
	ds_bpermute_b32 v10, v17, v10
	v_cndmask_b32_e32 v4, v4, v13, vcc
	ds_bpermute_b32 v12, v17, v12
	s_waitcnt lgkmcnt(3)
	v_add_f32_e32 v7, v7, v8
	s_waitcnt lgkmcnt(2)
	v_add_f32_e32 v4, v4, v9
	v_cndmask_b32_e32 v8, v14, v0, vcc
	v_cndmask_b32_e32 v9, v15, v1, vcc
	ds_bpermute_b32 v19, v17, v19
	ds_bpermute_b32 v8, v17, v8
	ds_bpermute_b32 v9, v17, v9
	v_cndmask_b32_e32 v5, v5, v16, vcc
	v_cndmask_b32_e32 v3, v11, v3, vcc
	s_waitcnt lgkmcnt(4)
	v_add_f32_e32 v5, v5, v10
	v_and_b32_e32 v10, 4, v77
	s_waitcnt lgkmcnt(3)
	v_add_f32_e32 v3, v3, v12
	v_cndmask_b32_e32 v0, v0, v14, vcc
	v_cmp_eq_u32_e64 s[10:11], 0, v10
	v_cndmask_b32_e32 v1, v1, v15, vcc
	s_waitcnt lgkmcnt(2)
	v_add_f32_e32 v6, v6, v19
	v_xor_b32_e32 v11, 16, v81
	v_cndmask_b32_e64 v10, v2, v4, s[10:11]
	s_waitcnt lgkmcnt(1)
	v_add_f32_e32 v0, v0, v8
	s_waitcnt lgkmcnt(0)
	v_add_f32_e32 v1, v1, v9
	v_cndmask_b32_e64 v2, v4, v2, s[10:11]
	v_cndmask_b32_e64 v4, v3, v5, s[10:11]
	v_cndmask_b32_e64 v3, v5, v3, s[10:11]
	ds_bpermute_b32 v4, v11, v4
	v_cndmask_b32_e64 v5, v6, v0, s[10:11]
	v_cndmask_b32_e64 v8, v7, v1, s[10:11]
	ds_bpermute_b32 v10, v11, v10
	ds_bpermute_b32 v5, v11, v5
	ds_bpermute_b32 v8, v11, v8
	s_waitcnt lgkmcnt(3)
	v_add_f32_e32 v3, v3, v4
	v_cndmask_b32_e64 v0, v0, v6, s[10:11]
	v_cndmask_b32_e64 v1, v1, v7, s[10:11]
	v_and_b32_e32 v4, 2, v77
	s_waitcnt lgkmcnt(2)
	v_add_f32_e32 v2, v2, v10
	s_waitcnt lgkmcnt(1)
	v_add_f32_e32 v0, v0, v5
	s_waitcnt lgkmcnt(0)
	v_add_f32_e32 v1, v1, v8
	v_cmp_eq_u32_e32 vcc, 0, v4
	v_xor_b32_e32 v5, 8, v81
	s_nop 0
	v_cndmask_b32_e32 v4, v2, v0, vcc
	v_cndmask_b32_e32 v6, v3, v1, vcc
	ds_bpermute_b32 v4, v5, v4
	ds_bpermute_b32 v5, v5, v6
	v_cndmask_b32_e32 v0, v0, v2, vcc
	v_cndmask_b32_e32 v1, v1, v3, vcc
	v_and_b32_e32 v3, 1, v77
	s_waitcnt lgkmcnt(1)
	v_add_f32_e32 v0, v0, v4
	s_waitcnt lgkmcnt(0)
	v_add_f32_e32 v1, v1, v5
	v_cmp_eq_u32_e32 vcc, 0, v3
	v_xor_b32_e32 v2, 4, v81
	s_nop 0
	v_cndmask_b32_e32 v3, v0, v1, vcc
	ds_bpermute_b32 v2, v2, v3
	v_cndmask_b32_e32 v0, v1, v0, vcc
	v_ashrrev_i32_e32 v1, 4, v77
	v_cmp_eq_u32_e32 vcc, 2, v1
	s_waitcnt lgkmcnt(0)
	v_add_f32_e32 v0, v0, v2
	v_cndmask_b32_e32 v2, v82, v80, vcc
	v_cmp_eq_u32_e32 vcc, 1, v1
	s_nop 1
	v_cndmask_b32_e32 v1, v2, v78, vcc
	v_cmp_gt_u32_e32 vcc, 16, v77
	s_nop 1
	v_cndmask_b32_e32 v1, v1, v76, vcc
	s_waitcnt vmcnt(0)
	v_fmac_f32_e32 v18, v1, v0
	v_add_u32_e32 v0, s96, v81
	ds_write_b32 v0, v18
	s_waitcnt lgkmcnt(0)
	s_and_saveexec_b64 s[44:45], s[8:9]
	s_cbranch_execz .LBB0_2563
	s_load_dwordx2 s[10:11], s[18:19], 0xa8
	v_add_u32_e32 v4, s96, v101
	s_waitcnt lgkmcnt(0)
	global_load_dwordx4 v[24:27], v33, s[10:11]
	global_load_dwordx4 v[16:19], v33, s[10:11] offset:16
	global_load_dwordx4 v[0:3], v33, s[10:11] offset:48
	global_load_dwordx4 v[8:11], v33, s[10:11] offset:32
	ds_read_b128 v[28:31], v4
	ds_read_b128 v[20:23], v4 offset:16
	s_waitcnt lgkmcnt(1)
	v_mul_f32_e32 v5, 0xbfb8aa3b, v28
	v_exp_f32_e32 v28, v5
	v_mul_f32_e32 v6, 0xbfb8aa3b, v29
	v_exp_f32_e32 v29, v6
	ds_read_b128 v[12:15], v4 offset:32
	ds_read_b128 v[4:7], v4 offset:48
	v_add_f32_e32 v28, 1.0, v28
	v_div_scale_f32 v44, s[10:11], v28, v28, 1.0
	v_add_f32_e32 v29, 1.0, v29
	v_rcp_f32_e32 v47, v44
	v_div_scale_f32 v46, s[10:11], v29, v29, 1.0
	v_rcp_f32_e32 v49, v46
	v_fma_f32 v50, -v44, v47, 1.0
	v_div_scale_f32 v45, vcc, 1.0, v28, 1.0
	v_fmac_f32_e32 v47, v50, v47
	v_fma_f32 v51, -v46, v49, 1.0
	v_mul_f32_e32 v50, v45, v47
	v_div_scale_f32 v48, s[10:11], 1.0, v29, 1.0
	v_fmac_f32_e32 v49, v51, v49
	v_fma_f32 v52, -v44, v50, v45
	v_mul_f32_e32 v51, v48, v49
	v_fmac_f32_e32 v50, v52, v47
	v_fma_f32 v53, -v46, v51, v48
	v_fma_f32 v44, -v44, v50, v45
	v_fmac_f32_e32 v51, v53, v49
	v_div_fmas_f32 v44, v44, v47, v50
	v_fma_f32 v45, -v46, v51, v48
	v_div_fixup_f32 v48, v44, v28, 1.0
	s_mov_b64 vcc, s[10:11]
	v_div_fmas_f32 v28, v45, v49, v51
	v_div_fixup_f32 v46, v28, v29, 1.0
	s_waitcnt vmcnt(3)
	v_add_f32_e32 v49, v24, v48
	v_cmp_lt_f32_e64 s[10:11], s55, v49
	v_add_f32_e32 v47, v25, v46
	v_mov_b32_e32 v24, v47
	v_cndmask_b32_e64 v25, v108, v49, s[10:11]
	v_cmp_ngt_f32_e32 vcc, v47, v25
	s_and_saveexec_b64 s[12:13], vcc
	s_cbranch_execz .LBB0_2428
	v_mov_b32_e32 v28, 0xf149f2ca
	v_cmp_gt_f32_e32 vcc, v47, v28
	s_and_saveexec_b64 s[14:15], vcc
	v_mov_b32_e32 v28, v47
	s_or_b64 exec, exec, s[14:15]
	v_mov_b32_e32 v24, v25
	v_mov_b32_e32 v25, v28
